# speedup vs baseline: 1.0211x; 1.0211x over previous
_Z11center_mainPKfPKcS0_Pf:
	s_load_dwordx4 s[4:7], s[0:1], 0x0
	s_load_dwordx2 s[8:9], s[0:1], 0x10
	s_and_b32 s3, s2, 7
	s_lshr_b32 s12, s2, 3
	v_lshrrev_b32_e32 v1, 6, v0
	v_and_b32_e32 v2, 63, v0
	v_bfe_u32 v3, v0, 3, 3
	v_and_b32_e32 v4, 7, v0
	v_lshrrev_b32_e32 v5, 7, v0
	v_bfe_u32 v6, v0, 6, 1
	v_lshl_or_b32 v7, v5, 3, v3
	v_lshlrev_b32_e32 v8, 10, v7
	v_lshl_or_b32 v8, v6, 9, v8
	v_lshl_or_b32 v242, v4, 4, v8
	v_lshlrev_b32_e32 v17, 15, v1
	v_lshl_or_b32 v243, v2, 5, v17
	v_lshlrev_b32_e32 v254, 3, v0
	s_lshl_b32 s13, s3, 22
	s_lshl_b32 s14, s12, 15
	s_add_u32 s13, s13, s14
	s_lshl_b32 s15, s3, 18
	s_lshl_b32 s28, s3, 12
	s_waitcnt lgkmcnt(0)
	s_add_u32 s16, s4, s13
	s_addc_u32 s17, s5, 0
	s_add_u32 s18, s16, 0x100000
	s_addc_u32 s19, s17, 0
	s_add_u32 s20, s16, 0x200000
	s_addc_u32 s21, s17, 0
	s_add_u32 s22, s16, 0x300000
	s_addc_u32 s23, s17, 0
	s_add_u32 s24, s6, s15
	s_addc_u32 s25, s7, 0
	s_add_u32 s8, s8, s28
	s_addc_u32 s9, s9, 0
	s_add_u32 s32, s24, 0x1000
	s_addc_u32 s33, s25, 0
	s_add_u32 s34, s24, 0x2000
	s_addc_u32 s35, s25, 0
	s_add_u32 s36, s24, 0x3000
	s_addc_u32 s37, s25, 0
	s_add_u32 s38, s24, 0x4000
	s_addc_u32 s39, s25, 0
	s_add_u32 s40, s24, 0x5000
	s_addc_u32 s41, s25, 0
	s_add_u32 s42, s24, 0x6000
	s_addc_u32 s43, s25, 0
	s_add_u32 s44, s24, 0x7000
	s_addc_u32 s45, s25, 0
	global_load_dwordx2 v[252:253], v254, s[8:9]
	global_load_dwordx4 v[146:149], v242, s[16:17] offset:0 nt
	global_load_dwordx4 v[150:153], v242, s[16:17] offset:128 nt
	global_load_dwordx4 v[154:157], v242, s[16:17] offset:256 nt
	global_load_dwordx4 v[158:161], v242, s[16:17] offset:384 nt
	global_load_dwordx4 v[34:37], v243, s[24:25] offset:0
	global_load_dwordx4 v[38:41], v243, s[24:25] offset:16
	global_load_dwordx4 v[26:29], v243, s[24:25] offset:2048
	global_load_dwordx4 v[30:33], v243, s[24:25] offset:2064
	global_load_dwordx4 v[50:53], v243, s[32:33] offset:0
	global_load_dwordx4 v[54:57], v243, s[32:33] offset:16
	global_load_dwordx4 v[42:45], v243, s[32:33] offset:2048
	global_load_dwordx4 v[46:49], v243, s[32:33] offset:2064
	global_load_dwordx4 v[18:21], v243, s[34:35] offset:0
	global_load_dwordx4 v[22:25], v243, s[34:35] offset:16
	global_load_dwordx4 v[130:133], v243, s[34:35] offset:2048
	global_load_dwordx4 v[134:137], v243, s[34:35] offset:2064
	global_load_dwordx4 v[122:125], v243, s[36:37] offset:0
	global_load_dwordx4 v[126:129], v243, s[36:37] offset:16
	global_load_dwordx4 v[138:141], v243, s[36:37] offset:2048
	global_load_dwordx4 v[142:145], v243, s[36:37] offset:2064
	global_load_dwordx4 v[98:101], v243, s[38:39] offset:0
	global_load_dwordx4 v[102:105], v243, s[38:39] offset:16
	global_load_dwordx4 v[90:93], v243, s[38:39] offset:2048
	global_load_dwordx4 v[94:97], v243, s[38:39] offset:2064
	global_load_dwordx4 v[114:117], v243, s[40:41] offset:0
	global_load_dwordx4 v[118:121], v243, s[40:41] offset:16
	global_load_dwordx4 v[106:109], v243, s[40:41] offset:2048
	global_load_dwordx4 v[110:113], v243, s[40:41] offset:2064
	global_load_dwordx4 v[58:61], v243, s[42:43] offset:0
	global_load_dwordx4 v[62:65], v243, s[42:43] offset:16
	global_load_dwordx4 v[66:69], v243, s[42:43] offset:2048
	global_load_dwordx4 v[70:73], v243, s[42:43] offset:2064
	global_load_dwordx4 v[74:77], v243, s[44:45] offset:0
	global_load_dwordx4 v[78:81], v243, s[44:45] offset:16
	global_load_dwordx4 v[82:85], v243, s[44:45] offset:2048
	global_load_dwordx4 v[86:89], v243, s[44:45] offset:2064
	v_mul_u32_u24_e32 v9, 0x110, v7
	v_lshl_add_u32 v9, v6, 7, v9
	v_lshl_add_u32 v244, v4, 4, v9
	v_lshlrev_b32_e32 v10, 6, v7
	v_lshl_or_b32 v10, v6, 5, v10
	v_lshl_or_b32 v245, v4, 2, v10
	v_and_b32_e32 v11, 31, v0
	v_bfe_u32 v12, v0, 5, 1
	v_mul_u32_u24_e32 v13, 0x110, v11
	v_lshl_add_u32 v246, v12, 5, v13
	v_lshlrev_b32_e32 v14, 9, v1
	v_lshl_or_b32 v247, v12, 4, v14
	v_xor_b32_e32 v15, 32, v2
	v_lshlrev_b32_e32 v248, 2, v15
	v_lshlrev_b32_e32 v16, 7, v1
	v_lshl_or_b32 v249, v11, 2, v16
	v_mov_b32_e32 v250, 0x7f7f7f7f
	s_waitcnt vmcnt(32)
	ds_write_b64 v254, v[252:253] offset:34816
	v_mul_f32_e32 v6, v146, v146
	v_mul_f32_e32 v7, v150, v150
	v_cvt_pk_fp8_f32 v2, v146, v147
	v_cvt_pk_fp8_f32 v3, v150, v151
	v_cvt_pk_fp8_f32 v4, v154, v155
	v_cvt_pk_fp8_f32 v5, v158, v159
	v_fmac_f32_e32 v6, v147, v147
	v_fmac_f32_e32 v7, v151, v151
	v_fmac_f32_e32 v6, v148, v148
	v_fmac_f32_e32 v7, v152, v152
	v_fmac_f32_e32 v6, v149, v149
	v_fmac_f32_e32 v7, v153, v153
	v_fmac_f32_e32 v6, v154, v154
	v_fmac_f32_e32 v7, v158, v158
	v_fmac_f32_e32 v6, v155, v155
	v_fmac_f32_e32 v7, v159, v159
	v_fmac_f32_e32 v6, v156, v156
	v_fmac_f32_e32 v7, v160, v160
	v_fmac_f32_e32 v6, v157, v157
	v_fmac_f32_e32 v7, v161, v161
	v_cvt_pk_fp8_f32 v2, v148, v149 op_sel:[0,0,1]
	v_cvt_pk_fp8_f32 v3, v152, v153 op_sel:[0,0,1]
	v_cvt_pk_fp8_f32 v4, v156, v157 op_sel:[0,0,1]
	v_cvt_pk_fp8_f32 v5, v160, v161 op_sel:[0,0,1]
	v_add_f32_e32 v6, v6, v7
	s_nop 0
	ds_write_b128 v244, v[2:5] offset:0
	ds_write_b32 v245, v6 offset:38912
	global_load_dwordx4 v[162:165], v242, s[18:19] offset:0 nt
	global_load_dwordx4 v[166:169], v242, s[18:19] offset:128 nt
	global_load_dwordx4 v[170:173], v242, s[18:19] offset:256 nt
	global_load_dwordx4 v[174:177], v242, s[18:19] offset:384 nt
	s_waitcnt lgkmcnt(0)
	s_barrier
	ds_read_b128 v[210:213], v246 offset:0
	ds_read_b128 v[214:217], v246 offset:16
	ds_read_b128 v[2:5], v247 offset:34816
	ds_read_b128 v[6:9], v247 offset:34848
	ds_read_b128 v[10:13], v247 offset:34880
	ds_read_b128 v[14:17], v247 offset:34912
	ds_read_b128 v[218:221], v246 offset:64
	ds_read_b128 v[222:225], v246 offset:80
	ds_read_b128 v[226:229], v246 offset:128
	ds_read_b128 v[230:233], v246 offset:144
	ds_read_b128 v[234:237], v246 offset:192
	ds_read_b128 v[238:241], v246 offset:208
	s_waitcnt vmcnt(34) lgkmcnt(6)
	v_mfma_scale_f32_32x32x64_f8f6f4 v[2:17], v[34:41], v[210:217], v[2:17], v250, v250 op_sel_hi:[0,0,0]
	s_waitcnt vmcnt(32) lgkmcnt(4)
	v_mfma_scale_f32_32x32x64_f8f6f4 v[2:17], v[26:33], v[218:225], v[2:17], v250, v250 op_sel_hi:[0,0,0]
	s_waitcnt vmcnt(30) lgkmcnt(2)
	v_mfma_scale_f32_32x32x64_f8f6f4 v[2:17], v[50:57], v[226:233], v[2:17], v250, v250 op_sel_hi:[0,0,0]
	s_waitcnt vmcnt(28) lgkmcnt(0)
	v_mfma_scale_f32_32x32x64_f8f6f4 v[2:17], v[42:49], v[234:241], v[2:17], v250, v250 op_sel_hi:[0,0,0]
	s_nop 15
	s_nop 3
	v_min3_f32 v2, v2, v3, v4
	v_min3_f32 v5, v5, v6, v7
	v_min3_f32 v8, v8, v9, v10
	v_min3_f32 v11, v11, v12, v13
	v_min3_f32 v14, v14, v15, v16
	v_min3_f32 v2, v2, v5, v8
	v_min3_f32 v11, v11, v14, v17
	v_min_f32_e32 v251, v2, v11
	ds_read_b128 v[2:5], v247 offset:34944
	ds_read_b128 v[6:9], v247 offset:34976
	ds_read_b128 v[10:13], v247 offset:35008
	ds_read_b128 v[14:17], v247 offset:35040
	s_waitcnt vmcnt(26) lgkmcnt(0)
	v_mfma_scale_f32_32x32x64_f8f6f4 v[2:17], v[18:25], v[210:217], v[2:17], v250, v250 op_sel_hi:[0,0,0]
	s_waitcnt vmcnt(24)
	v_mfma_scale_f32_32x32x64_f8f6f4 v[2:17], v[130:137], v[218:225], v[2:17], v250, v250 op_sel_hi:[0,0,0]
	s_waitcnt vmcnt(22)
	v_mfma_scale_f32_32x32x64_f8f6f4 v[2:17], v[122:129], v[226:233], v[2:17], v250, v250 op_sel_hi:[0,0,0]
	s_waitcnt vmcnt(20)
	v_mfma_scale_f32_32x32x64_f8f6f4 v[2:17], v[138:145], v[234:241], v[2:17], v250, v250 op_sel_hi:[0,0,0]
	s_nop 15
	s_nop 3
	v_min3_f32 v2, v2, v3, v4
	v_min3_f32 v5, v5, v6, v7
	v_min3_f32 v8, v8, v9, v10
	v_min3_f32 v11, v11, v12, v13
	v_min3_f32 v14, v14, v15, v16
	v_min3_f32 v2, v2, v5, v8
	v_min3_f32 v11, v11, v14, v17
	v_min3_f32 v251, v251, v2, v11
	ds_read_b128 v[2:5], v247 offset:35072
	ds_read_b128 v[6:9], v247 offset:35104
	ds_read_b128 v[10:13], v247 offset:35136
	ds_read_b128 v[14:17], v247 offset:35168
	s_waitcnt vmcnt(18) lgkmcnt(0)
	v_mfma_scale_f32_32x32x64_f8f6f4 v[2:17], v[98:105], v[210:217], v[2:17], v250, v250 op_sel_hi:[0,0,0]
	s_waitcnt vmcnt(16)
	v_mfma_scale_f32_32x32x64_f8f6f4 v[2:17], v[90:97], v[218:225], v[2:17], v250, v250 op_sel_hi:[0,0,0]
	s_waitcnt vmcnt(14)
	v_mfma_scale_f32_32x32x64_f8f6f4 v[2:17], v[114:121], v[226:233], v[2:17], v250, v250 op_sel_hi:[0,0,0]
	s_waitcnt vmcnt(12)
	v_mfma_scale_f32_32x32x64_f8f6f4 v[2:17], v[106:113], v[234:241], v[2:17], v250, v250 op_sel_hi:[0,0,0]
	s_nop 15
	s_nop 3
	v_min3_f32 v2, v2, v3, v4
	v_min3_f32 v5, v5, v6, v7
	v_min3_f32 v8, v8, v9, v10
	v_min3_f32 v11, v11, v12, v13
	v_min3_f32 v14, v14, v15, v16
	v_min3_f32 v2, v2, v5, v8
	v_min3_f32 v11, v11, v14, v17
	v_min3_f32 v251, v251, v2, v11
	ds_read_b128 v[2:5], v247 offset:35200
	ds_read_b128 v[6:9], v247 offset:35232
	ds_read_b128 v[10:13], v247 offset:35264
	ds_read_b128 v[14:17], v247 offset:35296
	s_waitcnt vmcnt(10) lgkmcnt(0)
	v_mfma_scale_f32_32x32x64_f8f6f4 v[2:17], v[58:65], v[210:217], v[2:17], v250, v250 op_sel_hi:[0,0,0]
	s_waitcnt vmcnt(8)
	v_mfma_scale_f32_32x32x64_f8f6f4 v[2:17], v[66:73], v[218:225], v[2:17], v250, v250 op_sel_hi:[0,0,0]
	s_waitcnt vmcnt(6)
	v_mfma_scale_f32_32x32x64_f8f6f4 v[2:17], v[74:81], v[226:233], v[2:17], v250, v250 op_sel_hi:[0,0,0]
	s_waitcnt vmcnt(4)
	v_mfma_scale_f32_32x32x64_f8f6f4 v[2:17], v[82:89], v[234:241], v[2:17], v250, v250 op_sel_hi:[0,0,0]
	s_nop 15
	s_nop 3
	v_min3_f32 v2, v2, v3, v4
	v_min3_f32 v5, v5, v6, v7
	v_min3_f32 v8, v8, v9, v10
	v_min3_f32 v11, v11, v12, v13
	v_min3_f32 v14, v14, v15, v16
	v_min3_f32 v2, v2, v5, v8
	v_min3_f32 v11, v11, v14, v17
	v_min3_f32 v251, v251, v2, v11
	ds_bpermute_b32 v3, v248, v251
	s_waitcnt lgkmcnt(0)
	v_min_f32_e32 v2, v251, v3
	ds_write_b32 v249, v2 offset:47104
	global_load_dwordx4 v[178:181], v242, s[20:21] offset:0 nt
	global_load_dwordx4 v[182:185], v242, s[20:21] offset:128 nt
	global_load_dwordx4 v[186:189], v242, s[20:21] offset:256 nt
	global_load_dwordx4 v[190:193], v242, s[20:21] offset:384 nt
	s_waitcnt vmcnt(4)
	v_mul_f32_e32 v6, v162, v162
	v_mul_f32_e32 v7, v166, v166
	v_cvt_pk_fp8_f32 v2, v162, v163
	v_cvt_pk_fp8_f32 v3, v166, v167
	v_cvt_pk_fp8_f32 v4, v170, v171
	v_cvt_pk_fp8_f32 v5, v174, v175
	v_fmac_f32_e32 v6, v163, v163
	v_fmac_f32_e32 v7, v167, v167
	v_fmac_f32_e32 v6, v164, v164
	v_fmac_f32_e32 v7, v168, v168
	v_fmac_f32_e32 v6, v165, v165
	v_fmac_f32_e32 v7, v169, v169
	v_fmac_f32_e32 v6, v170, v170
	v_fmac_f32_e32 v7, v174, v174
	v_fmac_f32_e32 v6, v171, v171
	v_fmac_f32_e32 v7, v175, v175
	v_fmac_f32_e32 v6, v172, v172
	v_fmac_f32_e32 v7, v176, v176
	v_fmac_f32_e32 v6, v173, v173
	v_fmac_f32_e32 v7, v177, v177
	v_cvt_pk_fp8_f32 v2, v164, v165 op_sel:[0,0,1]
	v_cvt_pk_fp8_f32 v3, v168, v169 op_sel:[0,0,1]
	v_cvt_pk_fp8_f32 v4, v172, v173 op_sel:[0,0,1]
	v_cvt_pk_fp8_f32 v5, v176, v177 op_sel:[0,0,1]
	v_add_f32_e32 v6, v6, v7
	s_nop 0
	ds_write_b128 v244, v[2:5] offset:8704
	ds_write_b32 v245, v6 offset:40960
	s_waitcnt lgkmcnt(0)
	s_barrier
	ds_read_b128 v[210:213], v246 offset:8704
	ds_read_b128 v[214:217], v246 offset:8720
	ds_read_b128 v[2:5], v247 offset:34816
	ds_read_b128 v[6:9], v247 offset:34848
	ds_read_b128 v[10:13], v247 offset:34880
	ds_read_b128 v[14:17], v247 offset:34912
	ds_read_b128 v[218:221], v246 offset:8768
	ds_read_b128 v[222:225], v246 offset:8784
	ds_read_b128 v[226:229], v246 offset:8832
	ds_read_b128 v[230:233], v246 offset:8848
	ds_read_b128 v[234:237], v246 offset:8896
	ds_read_b128 v[238:241], v246 offset:8912
	s_waitcnt lgkmcnt(6)
	v_mfma_scale_f32_32x32x64_f8f6f4 v[2:17], v[34:41], v[210:217], v[2:17], v250, v250 op_sel_hi:[0,0,0]
	s_waitcnt lgkmcnt(4)
	v_mfma_scale_f32_32x32x64_f8f6f4 v[2:17], v[26:33], v[218:225], v[2:17], v250, v250 op_sel_hi:[0,0,0]
	s_waitcnt lgkmcnt(2)
	v_mfma_scale_f32_32x32x64_f8f6f4 v[2:17], v[50:57], v[226:233], v[2:17], v250, v250 op_sel_hi:[0,0,0]
	s_waitcnt lgkmcnt(0)
	v_mfma_scale_f32_32x32x64_f8f6f4 v[2:17], v[42:49], v[234:241], v[2:17], v250, v250 op_sel_hi:[0,0,0]
	s_nop 15
	s_nop 3
	v_min3_f32 v2, v2, v3, v4
	v_min3_f32 v5, v5, v6, v7
	v_min3_f32 v8, v8, v9, v10
	v_min3_f32 v11, v11, v12, v13
	v_min3_f32 v14, v14, v15, v16
	v_min3_f32 v2, v2, v5, v8
	v_min3_f32 v11, v11, v14, v17
	v_min_f32_e32 v251, v2, v11
	ds_read_b128 v[2:5], v247 offset:34944
	ds_read_b128 v[6:9], v247 offset:34976
	ds_read_b128 v[10:13], v247 offset:35008
	ds_read_b128 v[14:17], v247 offset:35040
	s_waitcnt lgkmcnt(0)
	v_mfma_scale_f32_32x32x64_f8f6f4 v[2:17], v[18:25], v[210:217], v[2:17], v250, v250 op_sel_hi:[0,0,0]
	v_mfma_scale_f32_32x32x64_f8f6f4 v[2:17], v[130:137], v[218:225], v[2:17], v250, v250 op_sel_hi:[0,0,0]
	v_mfma_scale_f32_32x32x64_f8f6f4 v[2:17], v[122:129], v[226:233], v[2:17], v250, v250 op_sel_hi:[0,0,0]
	v_mfma_scale_f32_32x32x64_f8f6f4 v[2:17], v[138:145], v[234:241], v[2:17], v250, v250 op_sel_hi:[0,0,0]
	s_nop 15
	s_nop 3
	v_min3_f32 v2, v2, v3, v4
	v_min3_f32 v5, v5, v6, v7
	v_min3_f32 v8, v8, v9, v10
	v_min3_f32 v11, v11, v12, v13
	v_min3_f32 v14, v14, v15, v16
	v_min3_f32 v2, v2, v5, v8
	v_min3_f32 v11, v11, v14, v17
	v_min3_f32 v251, v251, v2, v11
	ds_read_b128 v[2:5], v247 offset:35072
	ds_read_b128 v[6:9], v247 offset:35104
	ds_read_b128 v[10:13], v247 offset:35136
	ds_read_b128 v[14:17], v247 offset:35168
	s_waitcnt lgkmcnt(0)
	v_mfma_scale_f32_32x32x64_f8f6f4 v[2:17], v[98:105], v[210:217], v[2:17], v250, v250 op_sel_hi:[0,0,0]
	v_mfma_scale_f32_32x32x64_f8f6f4 v[2:17], v[90:97], v[218:225], v[2:17], v250, v250 op_sel_hi:[0,0,0]
	v_mfma_scale_f32_32x32x64_f8f6f4 v[2:17], v[114:121], v[226:233], v[2:17], v250, v250 op_sel_hi:[0,0,0]
	v_mfma_scale_f32_32x32x64_f8f6f4 v[2:17], v[106:113], v[234:241], v[2:17], v250, v250 op_sel_hi:[0,0,0]
	s_nop 15
	s_nop 3
	v_min3_f32 v2, v2, v3, v4
	v_min3_f32 v5, v5, v6, v7
	v_min3_f32 v8, v8, v9, v10
	v_min3_f32 v11, v11, v12, v13
	v_min3_f32 v14, v14, v15, v16
	v_min3_f32 v2, v2, v5, v8
	v_min3_f32 v11, v11, v14, v17
	v_min3_f32 v251, v251, v2, v11
	ds_read_b128 v[2:5], v247 offset:35200
	ds_read_b128 v[6:9], v247 offset:35232
	ds_read_b128 v[10:13], v247 offset:35264
	ds_read_b128 v[14:17], v247 offset:35296
	s_waitcnt lgkmcnt(0)
	v_mfma_scale_f32_32x32x64_f8f6f4 v[2:17], v[58:65], v[210:217], v[2:17], v250, v250 op_sel_hi:[0,0,0]
	v_mfma_scale_f32_32x32x64_f8f6f4 v[2:17], v[66:73], v[218:225], v[2:17], v250, v250 op_sel_hi:[0,0,0]
	v_mfma_scale_f32_32x32x64_f8f6f4 v[2:17], v[74:81], v[226:233], v[2:17], v250, v250 op_sel_hi:[0,0,0]
	v_mfma_scale_f32_32x32x64_f8f6f4 v[2:17], v[82:89], v[234:241], v[2:17], v250, v250 op_sel_hi:[0,0,0]
	s_nop 15
	s_nop 3
	v_min3_f32 v2, v2, v3, v4
	v_min3_f32 v5, v5, v6, v7
	v_min3_f32 v8, v8, v9, v10
	v_min3_f32 v11, v11, v12, v13
	v_min3_f32 v14, v14, v15, v16
	v_min3_f32 v2, v2, v5, v8
	v_min3_f32 v11, v11, v14, v17
	v_min3_f32 v251, v251, v2, v11
	ds_bpermute_b32 v3, v248, v251
	s_waitcnt lgkmcnt(0)
	v_min_f32_e32 v2, v251, v3
	ds_write_b32 v249, v2 offset:48128
	global_load_dwordx4 v[194:197], v242, s[22:23] offset:0 nt
	global_load_dwordx4 v[198:201], v242, s[22:23] offset:128 nt
	global_load_dwordx4 v[202:205], v242, s[22:23] offset:256 nt
	global_load_dwordx4 v[206:209], v242, s[22:23] offset:384 nt
	s_waitcnt vmcnt(4)
	v_mul_f32_e32 v6, v178, v178
	v_mul_f32_e32 v7, v182, v182
	v_cvt_pk_fp8_f32 v2, v178, v179
	v_cvt_pk_fp8_f32 v3, v182, v183
	v_cvt_pk_fp8_f32 v4, v186, v187
	v_cvt_pk_fp8_f32 v5, v190, v191
	v_fmac_f32_e32 v6, v179, v179
	v_fmac_f32_e32 v7, v183, v183
	v_fmac_f32_e32 v6, v180, v180
	v_fmac_f32_e32 v7, v184, v184
	v_fmac_f32_e32 v6, v181, v181
	v_fmac_f32_e32 v7, v185, v185
	v_fmac_f32_e32 v6, v186, v186
	v_fmac_f32_e32 v7, v190, v190
	v_fmac_f32_e32 v6, v187, v187
	v_fmac_f32_e32 v7, v191, v191
	v_fmac_f32_e32 v6, v188, v188
	v_fmac_f32_e32 v7, v192, v192
	v_fmac_f32_e32 v6, v189, v189
	v_fmac_f32_e32 v7, v193, v193
	v_cvt_pk_fp8_f32 v2, v180, v181 op_sel:[0,0,1]
	v_cvt_pk_fp8_f32 v3, v184, v185 op_sel:[0,0,1]
	v_cvt_pk_fp8_f32 v4, v188, v189 op_sel:[0,0,1]
	v_cvt_pk_fp8_f32 v5, v192, v193 op_sel:[0,0,1]
	v_add_f32_e32 v6, v6, v7
	s_nop 0
	ds_write_b128 v244, v[2:5] offset:17408
	ds_write_b32 v245, v6 offset:43008
	s_waitcnt lgkmcnt(0)
	s_barrier
	ds_read_b128 v[210:213], v246 offset:17408
	ds_read_b128 v[214:217], v246 offset:17424
	ds_read_b128 v[2:5], v247 offset:34816
	ds_read_b128 v[6:9], v247 offset:34848
	ds_read_b128 v[10:13], v247 offset:34880
	ds_read_b128 v[14:17], v247 offset:34912
	ds_read_b128 v[218:221], v246 offset:17472
	ds_read_b128 v[222:225], v246 offset:17488
	ds_read_b128 v[226:229], v246 offset:17536
	ds_read_b128 v[230:233], v246 offset:17552
	ds_read_b128 v[234:237], v246 offset:17600
	ds_read_b128 v[238:241], v246 offset:17616
	s_waitcnt lgkmcnt(6)
	v_mfma_scale_f32_32x32x64_f8f6f4 v[2:17], v[34:41], v[210:217], v[2:17], v250, v250 op_sel_hi:[0,0,0]
	s_waitcnt lgkmcnt(4)
	v_mfma_scale_f32_32x32x64_f8f6f4 v[2:17], v[26:33], v[218:225], v[2:17], v250, v250 op_sel_hi:[0,0,0]
	s_waitcnt lgkmcnt(2)
	v_mfma_scale_f32_32x32x64_f8f6f4 v[2:17], v[50:57], v[226:233], v[2:17], v250, v250 op_sel_hi:[0,0,0]
	s_waitcnt lgkmcnt(0)
	v_mfma_scale_f32_32x32x64_f8f6f4 v[2:17], v[42:49], v[234:241], v[2:17], v250, v250 op_sel_hi:[0,0,0]
	s_nop 15
	s_nop 3
	v_min3_f32 v2, v2, v3, v4
	v_min3_f32 v5, v5, v6, v7
	v_min3_f32 v8, v8, v9, v10
	v_min3_f32 v11, v11, v12, v13
	v_min3_f32 v14, v14, v15, v16
	v_min3_f32 v2, v2, v5, v8
	v_min3_f32 v11, v11, v14, v17
	v_min_f32_e32 v251, v2, v11
	ds_read_b128 v[2:5], v247 offset:34944
	ds_read_b128 v[6:9], v247 offset:34976
	ds_read_b128 v[10:13], v247 offset:35008
	ds_read_b128 v[14:17], v247 offset:35040
	s_waitcnt lgkmcnt(0)
	v_mfma_scale_f32_32x32x64_f8f6f4 v[2:17], v[18:25], v[210:217], v[2:17], v250, v250 op_sel_hi:[0,0,0]
	v_mfma_scale_f32_32x32x64_f8f6f4 v[2:17], v[130:137], v[218:225], v[2:17], v250, v250 op_sel_hi:[0,0,0]
	v_mfma_scale_f32_32x32x64_f8f6f4 v[2:17], v[122:129], v[226:233], v[2:17], v250, v250 op_sel_hi:[0,0,0]
	v_mfma_scale_f32_32x32x64_f8f6f4 v[2:17], v[138:145], v[234:241], v[2:17], v250, v250 op_sel_hi:[0,0,0]
	s_nop 15
	s_nop 3
	v_min3_f32 v2, v2, v3, v4
	v_min3_f32 v5, v5, v6, v7
	v_min3_f32 v8, v8, v9, v10
	v_min3_f32 v11, v11, v12, v13
	v_min3_f32 v14, v14, v15, v16
	v_min3_f32 v2, v2, v5, v8
	v_min3_f32 v11, v11, v14, v17
	v_min3_f32 v251, v251, v2, v11
	ds_read_b128 v[2:5], v247 offset:35072
	ds_read_b128 v[6:9], v247 offset:35104
	ds_read_b128 v[10:13], v247 offset:35136
	ds_read_b128 v[14:17], v247 offset:35168
	s_waitcnt lgkmcnt(0)
	v_mfma_scale_f32_32x32x64_f8f6f4 v[2:17], v[98:105], v[210:217], v[2:17], v250, v250 op_sel_hi:[0,0,0]
	v_mfma_scale_f32_32x32x64_f8f6f4 v[2:17], v[90:97], v[218:225], v[2:17], v250, v250 op_sel_hi:[0,0,0]
	v_mfma_scale_f32_32x32x64_f8f6f4 v[2:17], v[114:121], v[226:233], v[2:17], v250, v250 op_sel_hi:[0,0,0]
	v_mfma_scale_f32_32x32x64_f8f6f4 v[2:17], v[106:113], v[234:241], v[2:17], v250, v250 op_sel_hi:[0,0,0]
	s_nop 15
	s_nop 3
	v_min3_f32 v2, v2, v3, v4
	v_min3_f32 v5, v5, v6, v7
	v_min3_f32 v8, v8, v9, v10
	v_min3_f32 v11, v11, v12, v13
	v_min3_f32 v14, v14, v15, v16
	v_min3_f32 v2, v2, v5, v8
	v_min3_f32 v11, v11, v14, v17
	v_min3_f32 v251, v251, v2, v11
	ds_read_b128 v[2:5], v247 offset:35200
	ds_read_b128 v[6:9], v247 offset:35232
	ds_read_b128 v[10:13], v247 offset:35264
	ds_read_b128 v[14:17], v247 offset:35296
	s_waitcnt lgkmcnt(0)
	v_mfma_scale_f32_32x32x64_f8f6f4 v[2:17], v[58:65], v[210:217], v[2:17], v250, v250 op_sel_hi:[0,0,0]
	v_mfma_scale_f32_32x32x64_f8f6f4 v[2:17], v[66:73], v[218:225], v[2:17], v250, v250 op_sel_hi:[0,0,0]
	v_mfma_scale_f32_32x32x64_f8f6f4 v[2:17], v[74:81], v[226:233], v[2:17], v250, v250 op_sel_hi:[0,0,0]
	v_mfma_scale_f32_32x32x64_f8f6f4 v[2:17], v[82:89], v[234:241], v[2:17], v250, v250 op_sel_hi:[0,0,0]
	s_nop 15
	s_nop 3
	v_min3_f32 v2, v2, v3, v4
	v_min3_f32 v5, v5, v6, v7
	v_min3_f32 v8, v8, v9, v10
	v_min3_f32 v11, v11, v12, v13
	v_min3_f32 v14, v14, v15, v16
	v_min3_f32 v2, v2, v5, v8
	v_min3_f32 v11, v11, v14, v17
	v_min3_f32 v251, v251, v2, v11
	ds_bpermute_b32 v3, v248, v251
	s_waitcnt lgkmcnt(0)
	v_min_f32_e32 v2, v251, v3
	ds_write_b32 v249, v2 offset:49152
	s_waitcnt vmcnt(0)
	v_mul_f32_e32 v6, v194, v194
	v_mul_f32_e32 v7, v198, v198
	v_cvt_pk_fp8_f32 v2, v194, v195
	v_cvt_pk_fp8_f32 v3, v198, v199
	v_cvt_pk_fp8_f32 v4, v202, v203
	v_cvt_pk_fp8_f32 v5, v206, v207
	v_fmac_f32_e32 v6, v195, v195
	v_fmac_f32_e32 v7, v199, v199
	v_fmac_f32_e32 v6, v196, v196
	v_fmac_f32_e32 v7, v200, v200
	v_fmac_f32_e32 v6, v197, v197
	v_fmac_f32_e32 v7, v201, v201
	v_fmac_f32_e32 v6, v202, v202
	v_fmac_f32_e32 v7, v206, v206
	v_fmac_f32_e32 v6, v203, v203
	v_fmac_f32_e32 v7, v207, v207
	v_fmac_f32_e32 v6, v204, v204
	v_fmac_f32_e32 v7, v208, v208
	v_fmac_f32_e32 v6, v205, v205
	v_fmac_f32_e32 v7, v209, v209
	v_cvt_pk_fp8_f32 v2, v196, v197 op_sel:[0,0,1]
	v_cvt_pk_fp8_f32 v3, v200, v201 op_sel:[0,0,1]
	v_cvt_pk_fp8_f32 v4, v204, v205 op_sel:[0,0,1]
	v_cvt_pk_fp8_f32 v5, v208, v209 op_sel:[0,0,1]
	v_add_f32_e32 v6, v6, v7
	s_nop 0
	ds_write_b128 v244, v[2:5] offset:26112
	ds_write_b32 v245, v6 offset:45056
	s_waitcnt lgkmcnt(0)
	s_barrier
	ds_read_b128 v[210:213], v246 offset:26112
	ds_read_b128 v[214:217], v246 offset:26128
	ds_read_b128 v[2:5], v247 offset:34816
	ds_read_b128 v[6:9], v247 offset:34848
	ds_read_b128 v[10:13], v247 offset:34880
	ds_read_b128 v[14:17], v247 offset:34912
	ds_read_b128 v[218:221], v246 offset:26176
	ds_read_b128 v[222:225], v246 offset:26192
	ds_read_b128 v[226:229], v246 offset:26240
	ds_read_b128 v[230:233], v246 offset:26256
	ds_read_b128 v[234:237], v246 offset:26304
	ds_read_b128 v[238:241], v246 offset:26320
	s_waitcnt lgkmcnt(6)
	v_mfma_scale_f32_32x32x64_f8f6f4 v[2:17], v[34:41], v[210:217], v[2:17], v250, v250 op_sel_hi:[0,0,0]
	s_waitcnt lgkmcnt(4)
	v_mfma_scale_f32_32x32x64_f8f6f4 v[2:17], v[26:33], v[218:225], v[2:17], v250, v250 op_sel_hi:[0,0,0]
	s_waitcnt lgkmcnt(2)
	v_mfma_scale_f32_32x32x64_f8f6f4 v[2:17], v[50:57], v[226:233], v[2:17], v250, v250 op_sel_hi:[0,0,0]
	s_waitcnt lgkmcnt(0)
	v_mfma_scale_f32_32x32x64_f8f6f4 v[2:17], v[42:49], v[234:241], v[2:17], v250, v250 op_sel_hi:[0,0,0]
	s_nop 15
	s_nop 3
	v_min3_f32 v2, v2, v3, v4
	v_min3_f32 v5, v5, v6, v7
	v_min3_f32 v8, v8, v9, v10
	v_min3_f32 v11, v11, v12, v13
	v_min3_f32 v14, v14, v15, v16
	v_min3_f32 v2, v2, v5, v8
	v_min3_f32 v11, v11, v14, v17
	v_min_f32_e32 v251, v2, v11
	ds_read_b128 v[2:5], v247 offset:34944
	ds_read_b128 v[6:9], v247 offset:34976
	ds_read_b128 v[10:13], v247 offset:35008
	ds_read_b128 v[14:17], v247 offset:35040
	s_waitcnt lgkmcnt(0)
	v_mfma_scale_f32_32x32x64_f8f6f4 v[2:17], v[18:25], v[210:217], v[2:17], v250, v250 op_sel_hi:[0,0,0]
	v_mfma_scale_f32_32x32x64_f8f6f4 v[2:17], v[130:137], v[218:225], v[2:17], v250, v250 op_sel_hi:[0,0,0]
	v_mfma_scale_f32_32x32x64_f8f6f4 v[2:17], v[122:129], v[226:233], v[2:17], v250, v250 op_sel_hi:[0,0,0]
	v_mfma_scale_f32_32x32x64_f8f6f4 v[2:17], v[138:145], v[234:241], v[2:17], v250, v250 op_sel_hi:[0,0,0]
	s_nop 15
	s_nop 3
	v_min3_f32 v2, v2, v3, v4
	v_min3_f32 v5, v5, v6, v7
	v_min3_f32 v8, v8, v9, v10
	v_min3_f32 v11, v11, v12, v13
	v_min3_f32 v14, v14, v15, v16
	v_min3_f32 v2, v2, v5, v8
	v_min3_f32 v11, v11, v14, v17
	v_min3_f32 v251, v251, v2, v11
	ds_read_b128 v[2:5], v247 offset:35072
	ds_read_b128 v[6:9], v247 offset:35104
	ds_read_b128 v[10:13], v247 offset:35136
	ds_read_b128 v[14:17], v247 offset:35168
	s_waitcnt lgkmcnt(0)
	v_mfma_scale_f32_32x32x64_f8f6f4 v[2:17], v[98:105], v[210:217], v[2:17], v250, v250 op_sel_hi:[0,0,0]
	v_mfma_scale_f32_32x32x64_f8f6f4 v[2:17], v[90:97], v[218:225], v[2:17], v250, v250 op_sel_hi:[0,0,0]
	v_mfma_scale_f32_32x32x64_f8f6f4 v[2:17], v[114:121], v[226:233], v[2:17], v250, v250 op_sel_hi:[0,0,0]
	v_mfma_scale_f32_32x32x64_f8f6f4 v[2:17], v[106:113], v[234:241], v[2:17], v250, v250 op_sel_hi:[0,0,0]
	s_nop 15
	s_nop 3
	v_min3_f32 v2, v2, v3, v4
	v_min3_f32 v5, v5, v6, v7
	v_min3_f32 v8, v8, v9, v10
	v_min3_f32 v11, v11, v12, v13
	v_min3_f32 v14, v14, v15, v16
	v_min3_f32 v2, v2, v5, v8
	v_min3_f32 v11, v11, v14, v17
	v_min3_f32 v251, v251, v2, v11
	ds_read_b128 v[2:5], v247 offset:35200
	ds_read_b128 v[6:9], v247 offset:35232
	ds_read_b128 v[10:13], v247 offset:35264
	ds_read_b128 v[14:17], v247 offset:35296
	s_waitcnt lgkmcnt(0)
	v_mfma_scale_f32_32x32x64_f8f6f4 v[2:17], v[58:65], v[210:217], v[2:17], v250, v250 op_sel_hi:[0,0,0]
	v_mfma_scale_f32_32x32x64_f8f6f4 v[2:17], v[66:73], v[218:225], v[2:17], v250, v250 op_sel_hi:[0,0,0]
	v_mfma_scale_f32_32x32x64_f8f6f4 v[2:17], v[74:81], v[226:233], v[2:17], v250, v250 op_sel_hi:[0,0,0]
	v_mfma_scale_f32_32x32x64_f8f6f4 v[2:17], v[82:89], v[234:241], v[2:17], v250, v250 op_sel_hi:[0,0,0]
	s_nop 15
	s_nop 3
	v_min3_f32 v2, v2, v3, v4
	v_min3_f32 v5, v5, v6, v7
	v_min3_f32 v8, v8, v9, v10
	v_min3_f32 v11, v11, v12, v13
	v_min3_f32 v14, v14, v15, v16
	v_min3_f32 v2, v2, v5, v8
	v_min3_f32 v11, v11, v14, v17
	v_min3_f32 v251, v251, v2, v11
	ds_bpermute_b32 v3, v248, v251
	s_waitcnt lgkmcnt(0)
	v_min_f32_e32 v2, v251, v3
	ds_write_b32 v249, v2 offset:50176
	v_and_b32_e32 v182, 63, v0
	v_lshlrev_b32_e32 v183, 5, v0
	v_and_b32_e32 v184, 31, v0
	v_and_b32_e32 v185, 63, v0
	v_mov_b32_e32 v186, 64
	v_mov_b32_e32 v187, v248
	s_movk_i32 s2, 0x80
	v_cmp_gt_u32_e32 vcc, s2, v0
	v_mov_b32_e32 v2, 0
	s_waitcnt lgkmcnt(0)
	s_barrier
	s_and_saveexec_b64 s[4:5], vcc
	s_cbranch_execz .LBB1_10
	v_lshlrev_b32_e32 v2, 2, v184
	s_movk_i32 s2, 0xc00
	v_and_or_b32 v2, v183, s2, v2
	v_add_u32_e32 v8, 0xb800, v2
	ds_read2_b32 v[2:3], v8 offset1:32
	ds_read2_b32 v[4:5], v8 offset0:64 offset1:96
	ds_read2_b32 v[6:7], v8 offset0:192 offset1:224
	v_lshlrev_b32_e32 v14, 6, v0
	s_mov_b32 s2, 0xf800000
	s_waitcnt lgkmcnt(2)
	v_max_f32_e32 v3, v3, v3
	v_max_f32_e32 v2, v2, v2
	v_min_f32_e32 v10, v2, v3
	ds_read2_b32 v[2:3], v8 offset0:128 offset1:160
	s_waitcnt lgkmcnt(2)
	v_max_f32_e32 v5, v5, v5
	v_max_f32_e32 v4, v4, v4
	v_min_f32_e32 v11, v4, v5
	s_waitcnt lgkmcnt(1)
	v_max_f32_e32 v4, v7, v7
	v_max_f32_e32 v5, v6, v6
	v_min_f32_e32 v4, v5, v4
	s_waitcnt lgkmcnt(0)
	v_min3_f32 v12, v2, v3, v4
	ds_read_b128 v[2:5], v14 offset:38912
	ds_read_b128 v[6:9], v14 offset:38944
	v_min3_f32 v20, v10, v11, v12
	ds_read_b128 v[10:13], v14 offset:38928
	ds_read_b128 v[14:17], v14 offset:38960
	s_waitcnt lgkmcnt(3)
	v_mov_b32_e32 v18, v2
	s_waitcnt lgkmcnt(2)
	v_mov_b32_e32 v19, v6
	v_mov_b32_e32 v6, v3
	v_pk_add_f32 v[2:3], v[18:19], v[6:7]
	v_mov_b32_e32 v6, v4
	v_mov_b32_e32 v7, v8
	v_mov_b32_e32 v8, v5
	v_pk_add_f32 v[4:5], v[6:7], v[8:9]
	s_waitcnt lgkmcnt(1)
	v_mov_b32_e32 v6, v12
	v_pk_add_f32 v[2:3], v[2:3], v[4:5]
	v_mov_b32_e32 v4, v10
	s_waitcnt lgkmcnt(0)
	v_mov_b32_e32 v5, v14
	v_mov_b32_e32 v14, v11
	v_mov_b32_e32 v7, v16
	v_mov_b32_e32 v16, v13
	v_pk_add_f32 v[4:5], v[4:5], v[14:15]
	v_pk_add_f32 v[6:7], v[6:7], v[16:17]
	s_nop 0
	v_pk_add_f32 v[4:5], v[4:5], v[6:7]
	s_nop 0
	v_pk_add_f32 v[2:3], v[2:3], v[4:5]
	s_nop 0
	v_add_f32_e32 v2, v2, v3
	v_add_f32_e32 v2, v20, v2
	v_max_f32_e32 v2, 0, v2
	v_mul_f32_e32 v3, 0x4f800000, v2
	v_cmp_gt_f32_e32 vcc, s2, v2
	s_nop 1
	v_cndmask_b32_e32 v2, v2, v3, vcc
	v_sqrt_f32_e32 v3, v2
	s_nop 0
	v_add_u32_e32 v4, -1, v3
	v_fma_f32 v5, -v4, v3, v2
	v_cmp_ge_f32_e64 s[2:3], 0, v5
	v_add_u32_e32 v5, 1, v3
	s_nop 0
	v_cndmask_b32_e64 v4, v3, v4, s[2:3]
	v_fma_f32 v3, -v5, v3, v2
	v_cmp_lt_f32_e64 s[2:3], 0, v3
	s_nop 1
	v_cndmask_b32_e64 v3, v4, v5, s[2:3]
	v_mul_f32_e32 v4, 0x37800000, v3
	v_cndmask_b32_e32 v3, v3, v4, vcc
	v_mov_b32_e32 v4, 0x260
	v_cmp_class_f32_e32 vcc, v2, v4
	s_nop 1
	v_cndmask_b32_e32 v2, v3, v2, vcc

	.amdhsa_kernel _Z11center_mainPKfPKcS0_Pf
		.amdhsa_group_segment_fixed_size 51232
		.amdhsa_private_segment_fixed_size 0
		.amdhsa_kernarg_size 32
		.amdhsa_user_sgpr_count 2
		.amdhsa_user_sgpr_dispatch_ptr 0
		.amdhsa_user_sgpr_queue_ptr 0
		.amdhsa_user_sgpr_kernarg_segment_ptr 1
		.amdhsa_user_sgpr_dispatch_id 0
		.amdhsa_user_sgpr_kernarg_preload_length 0
		.amdhsa_user_sgpr_kernarg_preload_offset 0
		.amdhsa_user_sgpr_private_segment_size 0
		.amdhsa_uses_dynamic_stack 0
		.amdhsa_enable_private_segment 0
		.amdhsa_system_sgpr_workgroup_id_x 1
		.amdhsa_system_sgpr_workgroup_id_y 0
		.amdhsa_system_sgpr_workgroup_id_z 0
		.amdhsa_system_sgpr_workgroup_info 0
		.amdhsa_system_vgpr_workitem_id 0
		.amdhsa_next_free_vgpr 256
		.amdhsa_next_free_sgpr 91
		.amdhsa_accum_offset 256
		.amdhsa_reserve_vcc 1
		.amdhsa_float_round_mode_32 0
		.amdhsa_float_round_mode_16_64 0
		.amdhsa_float_denorm_mode_32 3
		.amdhsa_float_denorm_mode_16_64 3
		.amdhsa_dx10_clamp 1
		.amdhsa_ieee_mode 1
		.amdhsa_fp16_overflow 0
		.amdhsa_tg_split 0
		.amdhsa_exception_fp_ieee_invalid_op 0
		.amdhsa_exception_fp_denorm_src 0
		.amdhsa_exception_fp_ieee_div_zero 0
		.amdhsa_exception_fp_ieee_overflow 0
		.amdhsa_exception_fp_ieee_underflow 0
		.amdhsa_exception_fp_ieee_inexact 0
		.amdhsa_exception_int_div_zero 0
	.end_amdhsa_kernel

.Lfunc_end1:
	.size	_Z11center_mainPKfPKcS0_Pf, .Lfunc_end1-_Z11center_mainPKfPKcS0_Pf
	.set _Z11center_mainPKfPKcS0_Pf.num_vgpr, 256
	.set _Z11center_mainPKfPKcS0_Pf.num_agpr, 0
	.set _Z11center_mainPKfPKcS0_Pf.numbered_sgpr, 12
	.set _Z11center_mainPKfPKcS0_Pf.num_named_barrier, 0
	.set _Z11center_mainPKfPKcS0_Pf.private_seg_size, 0
	.set _Z11center_mainPKfPKcS0_Pf.uses_vcc, 1
	.set _Z11center_mainPKfPKcS0_Pf.uses_flat_scratch, 0
	.set _Z11center_mainPKfPKcS0_Pf.has_dyn_sized_stack, 0
	.set _Z11center_mainPKfPKcS0_Pf.has_recursion, 0
	.set _Z11center_mainPKfPKcS0_Pf.has_indirect_call, 0

amdhsa.kernels:
  - .agpr_count:     0
    .args:
      - .actual_access:  read_only
        .address_space:  global
        .offset:         0
        .size:           8
        .value_kind:     global_buffer
      - .actual_access:  write_only
        .address_space:  global
        .offset:         8
        .size:           8
        .value_kind:     global_buffer
      - .actual_access:  write_only
        .address_space:  global
        .offset:         16
        .size:           8
        .value_kind:     global_buffer
      - .actual_access:  write_only
        .address_space:  global
        .offset:         24
        .size:           8
        .value_kind:     global_buffer
    .group_segment_fixed_size: 8704
    .kernarg_segment_align: 8
    .kernarg_segment_size: 32
    .language:       OpenCL C
    .language_version:
      - 2
      - 0
    .max_flat_workgroup_size: 64
    .name:           _Z11center_prepPKfPcPfS2_
    .private_segment_fixed_size: 0
    .sgpr_count:     18
    .sgpr_spill_count: 0
    .symbol:         _Z11center_prepPKfPcPfS2_.kd
    .uniform_work_group_size: 1
    .uses_dynamic_stack: false
    .vgpr_count:     123
    .vgpr_spill_count: 0
    .wavefront_size: 64
  - .agpr_count:     0
    .args:
      - .actual_access:  read_only
        .address_space:  global
        .offset:         0
        .size:           8
        .value_kind:     global_buffer
      - .actual_access:  read_only
        .address_space:  global
        .offset:         8
        .size:           8
        .value_kind:     global_buffer
      - .actual_access:  read_only
        .address_space:  global
        .offset:         16
        .size:           8
        .value_kind:     global_buffer
      - .address_space:  global
        .offset:         24
        .size:           8
        .value_kind:     global_buffer
    .group_segment_fixed_size: 51232
    .kernarg_segment_align: 8
    .kernarg_segment_size: 32
    .language:       OpenCL C
    .language_version:
      - 2
      - 0
    .max_flat_workgroup_size: 512
    .name:           _Z11center_mainPKfPKcS0_Pf
    .private_segment_fixed_size: 0
    .sgpr_count:     18
    .sgpr_spill_count: 0
    .symbol:         _Z11center_mainPKfPKcS0_Pf.kd
    .uniform_work_group_size: 1
    .uses_dynamic_stack: false
    .vgpr_count:     256
    .vgpr_spill_count: 0
    .wavefront_size: 64
